# attention work queues: one snapshot of the 8 per-XCD ticket counters when the own queue runs dry, exhausted queues skipped without a serial ticket atomic each
# baseline (speedup 1.0000x reference)
; __device__ __forceinline__ unsigned xb_xcc_id() { return (unsigned)__builtin_amdgcn_s_getreg((3 << 11) | 20) & 0xFu; }
; __device__ __forceinline__ void attn_phase(const Ctx& X, const bf16* __restrict__ proj, const float* __restrict__ km, const int* __restrict__ positions, const float* __restrict__ rel_bias, ...
;     ...
;     const unsigned myx = xb_xcc_id() & 7u;
;     for (unsigned xo = 0; xo < 8u; ++xo) {
;     const unsigned xq = (myx + xo) & 7u;
;     for (;; ++it) {
;         if (X.tid == 0) qslot[it & 1] = __hip_atomic_fetch_add(qctr + 64 + 64 * xq, 1u, RLX_AGENT);
;         __syncthreads();
;         const unsigned u = (unsigned)__builtin_amdgcn_readfirstlane((int)qslot[it & 1]);
;         if (u >= 96u) { ++it; break; }
.LBB0_917:
	s_add_u32 s34, s88, 0x34a02000
	s_addc_u32 s35, s89, 0
	s_add_u32 s36, s88, 0x34a02400
	s_addc_u32 s37, s89, 0
	s_add_u32 s38, s88, 0x34a02800
	s_addc_u32 s39, s89, 0
	s_add_u32 s40, s88, 0x34a01400
	s_addc_u32 s41, s89, 0
	s_add_u32 s42, s88, 0x34a01800
	s_waitcnt vmcnt(0)
	v_mbcnt_lo_u32_b32 v3, -1, 0
	s_addc_u32 s43, s89, 0
	v_mbcnt_hi_u32_b32 v213, -1, v3
	s_add_u32 s44, s88, 0x34a01c00
	s_mov_b32 s68, 0xfff50000
	v_and_b32_e32 v3, 64, v213
	s_getreg_b32 s29, hwreg(HW_REG_XCC_ID, 0, 4)
	s_addc_u32 s45, s89, 0
	s_mov_b32 s46, 0
	v_cmp_eq_u32_e64 s[4:5], 0, v206
	v_mov_b32_e32 v2, 0
	s_mov_b64 s[16:17], 0xb0000
	s_movk_i32 s47, 0x80
	s_mov_b64 s[14:15], 0x160000
	s_mov_b64 s[12:13], 0x210000
	s_add_i32 s48, 0, 0x15100
	s_mov_b64 s[30:31], 0x370000
	s_mov_b32 s69, -1
	s_mov_b32 s49, 0x41000000
	s_mov_b64 s[70:71], 0x2c0000
	v_add_u32_e32 v214, 64, v3
	v_xor_b32_e32 v215, 1, v213
	v_xor_b32_e32 v216, 2, v213
	v_xor_b32_e32 v217, 4, v213
	v_xor_b32_e32 v218, 8, v213
	v_xor_b32_e32 v219, 16, v213
	v_xor_b32_e32 v220, 32, v213
	v_mov_b32_e32 v221, 0xff800000
	v_mov_b32_e32 v222, 0x80
	v_mov_b32_e32 v223, 0xb0000
	s_mov_b32 s99, 0
	s_branch .LBB0_919
.LBB0_918:
	s_cmp_lg_u32 s46, 0
	s_cbranch_scc1 .Lqsnap_done0
	s_cmp_eq_u64 s[4:5], 0
	s_cbranch_scc1 .Lqsnap_wait0
	v_mbcnt_lo_u32_b32 v3, -1, 0
	v_mbcnt_hi_u32_b32 v3, -1, v3
	v_lshlrev_b32_e32 v4, 8, v3
	s_mov_b64 s[100:101], exec
	s_mov_b64 exec, 0xff
	global_load_dword v4, v4, s[88:89] offset:768 sc1
	s_waitcnt vmcnt(0)
	v_cmp_lt_u32_e32 vcc, 0x5f, v4
	s_mov_b64 exec, s[100:101]
	s_nop 1
	s_and_b32 s99, vcc_lo, 0xff
	v_mov_b32_e32 v3, s99
	v_mov_b32_e32 v4, 0x22060
	ds_write_b32 v4, v3
	s_waitcnt lgkmcnt(0)
.Lqsnap_wait0:
	s_barrier
	v_mov_b32_e32 v4, 0x22060
	ds_read_b32 v3, v4
	s_waitcnt lgkmcnt(0)
	v_readfirstlane_b32 s99, v3

; __device__ __forceinline__ void attn_phase(const Ctx& X, const bf16* __restrict__ proj, const float* __restrict__ km, const int* __restrict__ positions, const float* __restrict__ rel_bias, ...
;     ...
;     for (unsigned xo = 0; xo < 8u; ++xo) {
;     const unsigned xq = (myx + xo) & 7u;
;     for (;; ++it) {
;         if (X.tid == 0) qslot[it & 1] = __hip_atomic_fetch_add(qctr + 64 + 64 * xq, 1u, RLX_AGENT);
;         __syncthreads();
;         const unsigned u = (unsigned)__builtin_amdgcn_readfirstlane((int)qslot[it & 1]);
;         if (u >= 96u) { ++it; break; }
.LBB0_919:
	s_add_i32 s0, s46, s29
	s_and_b32 s50, s0, 7
	s_lshr_b32 s98, s99, s50
	s_and_b32 s98, s98, 1
	s_cmp_lg_u32 s98, 0
	s_cbranch_scc1 .LBB0_918
	s_lshl_b32 s0, s50, 8
	s_add_u32 s72, s88, s0
	s_addc_u32 s73, s89, 0
	s_lshl_b32 s51, s50, 1
	s_add_i32 s51, s51, 7
	s_mov_b32 s52, s53
	s_branch .LBB0_923

; __device__ __forceinline__ unsigned xb_xcc_id() { return (unsigned)__builtin_amdgcn_s_getreg((3 << 11) | 20) & 0xFu; }
; __device__ __forceinline__ void attn_phase(const Ctx& X, const bf16* __restrict__ proj, const float* __restrict__ km, const int* __restrict__ positions, const float* __restrict__ rel_bias, ...
;     ...
;     const unsigned myx = xb_xcc_id() & 7u;
;     for (unsigned xo = 0; xo < 8u; ++xo) {
;     const unsigned xq = (myx + xo) & 7u;
;     for (;; ++it) {
;         if (X.tid == 0) qslot[it & 1] = __hip_atomic_fetch_add(qctr + 64 + 64 * xq, 1u, RLX_AGENT);
;         __syncthreads();
;         const unsigned u = (unsigned)__builtin_amdgcn_readfirstlane((int)qslot[it & 1]);
;         if (u >= 96u) { ++it; break; }
.LBB0_2685:
	s_add_u32 s27, s88, 0x1300
	s_addc_u32 s28, s89, 0
	s_add_u32 s29, s88, 0x34a02000
	s_addc_u32 s34, s89, 0
	s_add_u32 s35, s88, 0x34a02400
	s_addc_u32 s40, s89, 0
	s_add_u32 s41, s88, 0x34a02800
	s_addc_u32 s42, s89, 0
	s_add_u32 s43, s88, 0x34a01400
	s_addc_u32 s44, s89, 0
	s_add_u32 s45, s88, 0x34a01800
	s_waitcnt vmcnt(0)
	v_mbcnt_lo_u32_b32 v3, -1, 0
	s_addc_u32 s46, s89, 0
	v_mbcnt_hi_u32_b32 v213, -1, v3
	s_add_u32 s47, s88, 0x34a01c00
	s_mov_b32 s54, 0xfff50000
	v_and_b32_e32 v3, 64, v213
	s_getreg_b32 s26, hwreg(HW_REG_XCC_ID, 0, 4)
	s_addc_u32 s48, s89, 0
	s_mov_b32 s49, 0
	v_cmp_eq_u32_e64 s[4:5], 0, v206
	v_mov_b32_e32 v2, 0
	s_mov_b64 s[16:17], 0xb0000
	s_movk_i32 s50, 0x80
	s_mov_b64 s[14:15], 0x160000
	s_mov_b64 s[52:53], 0x210000
	s_add_i32 s51, 0, 0x15100
	s_mov_b64 s[30:31], 0x370000
	s_mov_b32 s55, -1
	s_mov_b32 s61, 0x41000000
	s_mov_b64 s[56:57], 0x2c0000
	v_add_u32_e32 v214, 64, v3
	v_xor_b32_e32 v215, 1, v213
	v_xor_b32_e32 v216, 2, v213
	v_xor_b32_e32 v217, 4, v213
	v_xor_b32_e32 v218, 8, v213
	v_xor_b32_e32 v219, 16, v213
	v_xor_b32_e32 v220, 32, v213
	v_mov_b32_e32 v221, 0xff800000
	v_mov_b32_e32 v222, 0x80
	v_mov_b32_e32 v223, 0xb0000
	s_mov_b32 s99, 0
	s_branch .LBB0_2687
.LBB0_2686:
	s_cmp_lg_u32 s49, 0
	s_cbranch_scc1 .Lqsnap_done1
	s_cmp_eq_u64 s[4:5], 0
	s_cbranch_scc1 .Lqsnap_wait1
	v_mbcnt_lo_u32_b32 v3, -1, 0
	v_mbcnt_hi_u32_b32 v3, -1, v3
	v_lshlrev_b32_e32 v4, 8, v3
	v_add_u32_e32 v4, 0x1000, v4
	s_mov_b64 s[100:101], exec
	s_mov_b64 exec, 0xff
	global_load_dword v4, v4, s[88:89] offset:768 sc1
	s_waitcnt vmcnt(0)
	v_cmp_lt_u32_e32 vcc, 0x5f, v4
	s_mov_b64 exec, s[100:101]
	s_nop 1
	s_and_b32 s99, vcc_lo, 0xff
	v_mov_b32_e32 v3, s99
	v_mov_b32_e32 v4, 0x22060
	ds_write_b32 v4, v3
	s_waitcnt lgkmcnt(0)

; __device__ __forceinline__ void attn_phase(const Ctx& X, const bf16* __restrict__ proj, const float* __restrict__ km, const int* __restrict__ positions, const float* __restrict__ rel_bias, ...
;     ...
;     for (unsigned xo = 0; xo < 8u; ++xo) {
;     const unsigned xq = (myx + xo) & 7u;
;     for (;; ++it) {
;         if (X.tid == 0) qslot[it & 1] = __hip_atomic_fetch_add(qctr + 64 + 64 * xq, 1u, RLX_AGENT);
;         __syncthreads();
;         const unsigned u = (unsigned)__builtin_amdgcn_readfirstlane((int)qslot[it & 1]);
;         if (u >= 96u) { ++it; break; }
.LBB0_2687:
	s_add_i32 s0, s49, s26
	s_and_b32 s62, s0, 7
	s_lshr_b32 s98, s99, s62
	s_and_b32 s98, s98, 1
	s_cmp_lg_u32 s98, 0
	s_cbranch_scc1 .LBB0_2686
	s_lshl_b32 s0, s62, 8
	s_add_u32 s58, s27, s0
	s_addc_u32 s59, s28, 0
	s_lshl_b32 s63, s62, 1
	s_add_i32 s63, s63, 7
	s_mov_b32 s66, s67
	s_branch .LBB0_2691

; __global__ void __launch_bounds__(NWAVES * 64, 2) fwd(Args args) {
	.amdhsa_kernel _Z3fwd4Args
		.amdhsa_group_segment_fixed_size 0
		.amdhsa_private_segment_fixed_size 0
		.amdhsa_kernarg_size 504
		.amdhsa_user_sgpr_count 2
		.amdhsa_user_sgpr_dispatch_ptr 0
		.amdhsa_user_sgpr_queue_ptr 0
		.amdhsa_user_sgpr_kernarg_segment_ptr 1
		.amdhsa_user_sgpr_dispatch_id 0
		.amdhsa_user_sgpr_kernarg_preload_length 0
		.amdhsa_user_sgpr_kernarg_preload_offset 0
		.amdhsa_user_sgpr_private_segment_size 0
		.amdhsa_uses_dynamic_stack 0
		.amdhsa_enable_private_segment 0
		.amdhsa_system_sgpr_workgroup_id_x 1
		.amdhsa_system_sgpr_workgroup_id_y 0
		.amdhsa_system_sgpr_workgroup_id_z 0
		.amdhsa_system_sgpr_workgroup_info 0
		.amdhsa_system_vgpr_workitem_id 0
		.amdhsa_next_free_vgpr 256
		.amdhsa_next_free_sgpr 102
		.amdhsa_accum_offset 256
		.amdhsa_reserve_vcc 1
		.amdhsa_float_round_mode_32 0
		.amdhsa_float_round_mode_16_64 0
		.amdhsa_float_denorm_mode_32 3
		.amdhsa_float_denorm_mode_16_64 3
		.amdhsa_dx10_clamp 1
		.amdhsa_ieee_mode 1
		.amdhsa_fp16_overflow 0
		.amdhsa_tg_split 0
		.amdhsa_exception_fp_ieee_invalid_op 0
		.amdhsa_exception_fp_denorm_src 0
		.amdhsa_exception_fp_ieee_div_zero 0
		.amdhsa_exception_fp_ieee_overflow 0
		.amdhsa_exception_fp_ieee_underflow 0
		.amdhsa_exception_fp_ieee_inexact 0
		.amdhsa_exception_int_div_zero 0
	.end_amdhsa_kernel

; __global__ void __launch_bounds__(NWAVES * 64, 2) fwd(Args args) {
amdhsa.kernels:
  - .agpr_count:     0
    .args:
      - .offset:         0
        .size:           248
        .value_kind:     by_value
      - .offset:         248
        .size:           4
        .value_kind:     hidden_block_count_x
      - .offset:         252
        .size:           4
        .value_kind:     hidden_block_count_y
      - .offset:         256
        .size:           4
        .value_kind:     hidden_block_count_z
      - .offset:         260
        .size:           2
        .value_kind:     hidden_group_size_x
      - .offset:         262
        .size:           2
        .value_kind:     hidden_group_size_y
      - .offset:         264
        .size:           2
        .value_kind:     hidden_group_size_z
      - .offset:         266
        .size:           2
        .value_kind:     hidden_remainder_x
      - .offset:         268
        .size:           2
        .value_kind:     hidden_remainder_y
      - .offset:         270
        .size:           2
        .value_kind:     hidden_remainder_z
      - .offset:         288
        .size:           8
        .value_kind:     hidden_global_offset_x
      - .offset:         296
        .size:           8
        .value_kind:     hidden_global_offset_y
      - .offset:         304
        .size:           8
        .value_kind:     hidden_global_offset_z
      - .offset:         312
        .size:           2
        .value_kind:     hidden_grid_dims
      - .offset:         368
        .size:           4
        .value_kind:     hidden_dynamic_lds_size
    .group_segment_fixed_size: 0
    .kernarg_segment_align: 8
    .kernarg_segment_size: 504
    .language:       OpenCL C
    .language_version:
      - 2
      - 0
    .max_flat_workgroup_size: 512
    .name:           _Z3fwd4Args
    .private_segment_fixed_size: 0
    .sgpr_count:     108
    .sgpr_spill_count: 100
    .symbol:         _Z3fwd4Args.kd
    .uniform_work_group_size: 1
    .uses_dynamic_stack: false
    .vgpr_count:     256
    .vgpr_spill_count: 0
    .wavefront_size: 64
